# speedup vs baseline: 1.0210x; 1.0101x over previous
.Lk3_epilogue:
	s_waitcnt vmcnt(0) lgkmcnt(0)
	s_nop 15
	s_lshl_b32 s39, s17, 2
	s_add_u32 s39, s39, s16
	s_lshl_b32 s39, s39, 7
	s_add_u32 s39, s39, s19
	s_lshl_b32 s39, s39, 14
	v_add_u32_e32 v216, s39, v223
	v_add_u32_e32 v217, 0x1000, v216
	v_add_u32_e32 v218, 0x2000, v216
	v_add_u32_e32 v219, 0x3000, v216
	v_mul_f32_e32 v0, 0x39800000, v0
	v_mul_f32_e32 v1, 0x39800000, v1
	v_mul_f32_e32 v2, 0x39800000, v2
	v_mul_f32_e32 v3, 0x39800000, v3
	v_mul_f32_e32 v4, 0x39800000, v4
	v_mul_f32_e32 v5, 0x39800000, v5
	v_mul_f32_e32 v6, 0x39800000, v6
	v_mul_f32_e32 v7, 0x39800000, v7
	v_mul_f32_e32 v8, 0x39800000, v8
	v_mul_f32_e32 v9, 0x39800000, v9
	v_mul_f32_e32 v10, 0x39800000, v10
	v_mul_f32_e32 v11, 0x39800000, v11
	v_mul_f32_e32 v12, 0x39800000, v12
	v_mul_f32_e32 v13, 0x39800000, v13
	v_mul_f32_e32 v14, 0x39800000, v14
	v_mul_f32_e32 v15, 0x39800000, v15
	v_cvt_pk_f16_f32 v144, v0, v1
	v_cvt_pk_f16_f32 v145, v2, v3
	v_cvt_pk_f16_f32 v146, v4, v5
	v_cvt_pk_f16_f32 v147, v6, v7
	global_store_dwordx4 v216, v[144:147], s[12:13] offset:0 sc1
	v_cvt_pk_f16_f32 v148, v8, v9
	v_cvt_pk_f16_f32 v149, v10, v11
	v_cvt_pk_f16_f32 v150, v12, v13
	v_cvt_pk_f16_f32 v151, v14, v15
	global_store_dwordx4 v216, v[148:151], s[12:13] offset:1024 sc1
	v_mul_f32_e32 v16, 0x39800000, v16
	v_mul_f32_e32 v17, 0x39800000, v17
	v_mul_f32_e32 v18, 0x39800000, v18
	v_mul_f32_e32 v19, 0x39800000, v19
	v_mul_f32_e32 v20, 0x39800000, v20
	v_mul_f32_e32 v21, 0x39800000, v21
	v_mul_f32_e32 v22, 0x39800000, v22
	v_mul_f32_e32 v23, 0x39800000, v23
	v_mul_f32_e32 v24, 0x39800000, v24
	v_mul_f32_e32 v25, 0x39800000, v25
	v_mul_f32_e32 v26, 0x39800000, v26
	v_mul_f32_e32 v27, 0x39800000, v27
	v_mul_f32_e32 v28, 0x39800000, v28
	v_mul_f32_e32 v29, 0x39800000, v29
	v_mul_f32_e32 v30, 0x39800000, v30
	v_mul_f32_e32 v31, 0x39800000, v31
	v_cvt_pk_f16_f32 v152, v16, v17
	v_cvt_pk_f16_f32 v153, v18, v19
	v_cvt_pk_f16_f32 v154, v20, v21
	v_cvt_pk_f16_f32 v155, v22, v23
	global_store_dwordx4 v216, v[152:155], s[12:13] offset:2048 sc1
	v_cvt_pk_f16_f32 v156, v24, v25
	v_cvt_pk_f16_f32 v157, v26, v27
	v_cvt_pk_f16_f32 v158, v28, v29
	v_cvt_pk_f16_f32 v159, v30, v31
	global_store_dwordx4 v216, v[156:159], s[12:13] offset:3072 sc1
	v_mul_f32_e32 v32, 0x39800000, v32
	v_mul_f32_e32 v33, 0x39800000, v33
	v_mul_f32_e32 v34, 0x39800000, v34
	v_mul_f32_e32 v35, 0x39800000, v35
	v_mul_f32_e32 v36, 0x39800000, v36
	v_mul_f32_e32 v37, 0x39800000, v37
	v_mul_f32_e32 v38, 0x39800000, v38
	v_mul_f32_e32 v39, 0x39800000, v39
	v_mul_f32_e32 v40, 0x39800000, v40
	v_mul_f32_e32 v41, 0x39800000, v41
	v_mul_f32_e32 v42, 0x39800000, v42
	v_mul_f32_e32 v43, 0x39800000, v43
	v_mul_f32_e32 v44, 0x39800000, v44
	v_mul_f32_e32 v45, 0x39800000, v45
	v_mul_f32_e32 v46, 0x39800000, v46
	v_mul_f32_e32 v47, 0x39800000, v47
	v_cvt_pk_f16_f32 v160, v32, v33
	v_cvt_pk_f16_f32 v161, v34, v35
	v_cvt_pk_f16_f32 v162, v36, v37
	v_cvt_pk_f16_f32 v163, v38, v39
	global_store_dwordx4 v217, v[160:163], s[12:13] offset:0 sc1
	v_cvt_pk_f16_f32 v164, v40, v41
	v_cvt_pk_f16_f32 v165, v42, v43
	v_cvt_pk_f16_f32 v166, v44, v45
	v_cvt_pk_f16_f32 v167, v46, v47
	global_store_dwordx4 v217, v[164:167], s[12:13] offset:1024 sc1
	v_mul_f32_e32 v48, 0x39800000, v48
	v_mul_f32_e32 v49, 0x39800000, v49
	v_mul_f32_e32 v50, 0x39800000, v50
	v_mul_f32_e32 v51, 0x39800000, v51
	v_mul_f32_e32 v52, 0x39800000, v52
	v_mul_f32_e32 v53, 0x39800000, v53
	v_mul_f32_e32 v54, 0x39800000, v54
	v_mul_f32_e32 v55, 0x39800000, v55
	v_mul_f32_e32 v56, 0x39800000, v56
	v_mul_f32_e32 v57, 0x39800000, v57
	v_mul_f32_e32 v58, 0x39800000, v58
	v_mul_f32_e32 v59, 0x39800000, v59
	v_mul_f32_e32 v60, 0x39800000, v60
	v_mul_f32_e32 v61, 0x39800000, v61
	v_mul_f32_e32 v62, 0x39800000, v62
	v_mul_f32_e32 v63, 0x39800000, v63
	v_cvt_pk_f16_f32 v168, v48, v49
	v_cvt_pk_f16_f32 v169, v50, v51
	v_cvt_pk_f16_f32 v170, v52, v53
	v_cvt_pk_f16_f32 v171, v54, v55
	global_store_dwordx4 v217, v[168:171], s[12:13] offset:2048 sc1
	v_cvt_pk_f16_f32 v172, v56, v57
	v_cvt_pk_f16_f32 v173, v58, v59
	v_cvt_pk_f16_f32 v174, v60, v61
	v_cvt_pk_f16_f32 v175, v62, v63
	global_store_dwordx4 v217, v[172:175], s[12:13] offset:3072 sc1
	v_mul_f32_e32 v64, 0x39800000, v64
	v_mul_f32_e32 v65, 0x39800000, v65
	v_mul_f32_e32 v66, 0x39800000, v66
	v_mul_f32_e32 v67, 0x39800000, v67
	v_mul_f32_e32 v68, 0x39800000, v68
	v_mul_f32_e32 v69, 0x39800000, v69
	v_mul_f32_e32 v70, 0x39800000, v70
	v_mul_f32_e32 v71, 0x39800000, v71
	v_mul_f32_e32 v72, 0x39800000, v72
	v_mul_f32_e32 v73, 0x39800000, v73
	v_mul_f32_e32 v74, 0x39800000, v74
	v_mul_f32_e32 v75, 0x39800000, v75
	v_mul_f32_e32 v76, 0x39800000, v76
	v_mul_f32_e32 v77, 0x39800000, v77
	v_mul_f32_e32 v78, 0x39800000, v78
	v_mul_f32_e32 v79, 0x39800000, v79
	v_cvt_pk_f16_f32 v176, v64, v65
	v_cvt_pk_f16_f32 v177, v66, v67
	v_cvt_pk_f16_f32 v178, v68, v69
	v_cvt_pk_f16_f32 v179, v70, v71
	global_store_dwordx4 v218, v[176:179], s[12:13] offset:0 sc1
	v_cvt_pk_f16_f32 v180, v72, v73
	v_cvt_pk_f16_f32 v181, v74, v75
	v_cvt_pk_f16_f32 v182, v76, v77
	v_cvt_pk_f16_f32 v183, v78, v79
	global_store_dwordx4 v218, v[180:183], s[12:13] offset:1024 sc1
	v_mul_f32_e32 v80, 0x39800000, v80
	v_mul_f32_e32 v81, 0x39800000, v81
	v_mul_f32_e32 v82, 0x39800000, v82
	v_mul_f32_e32 v83, 0x39800000, v83
	v_mul_f32_e32 v84, 0x39800000, v84
	v_mul_f32_e32 v85, 0x39800000, v85
	v_mul_f32_e32 v86, 0x39800000, v86
	v_mul_f32_e32 v87, 0x39800000, v87
	v_mul_f32_e32 v88, 0x39800000, v88
	v_mul_f32_e32 v89, 0x39800000, v89
	v_mul_f32_e32 v90, 0x39800000, v90
	v_mul_f32_e32 v91, 0x39800000, v91
	v_mul_f32_e32 v92, 0x39800000, v92
	v_mul_f32_e32 v93, 0x39800000, v93
	v_mul_f32_e32 v94, 0x39800000, v94
	v_mul_f32_e32 v95, 0x39800000, v95
	v_cvt_pk_f16_f32 v184, v80, v81
	v_cvt_pk_f16_f32 v185, v82, v83
	v_cvt_pk_f16_f32 v186, v84, v85
	v_cvt_pk_f16_f32 v187, v86, v87
	global_store_dwordx4 v218, v[184:187], s[12:13] offset:2048 sc1
	v_cvt_pk_f16_f32 v188, v88, v89
	v_cvt_pk_f16_f32 v189, v90, v91
	v_cvt_pk_f16_f32 v190, v92, v93
	v_cvt_pk_f16_f32 v191, v94, v95
	global_store_dwordx4 v218, v[188:191], s[12:13] offset:3072 sc1
	v_mul_f32_e32 v96, 0x39800000, v96
	v_mul_f32_e32 v97, 0x39800000, v97
	v_mul_f32_e32 v98, 0x39800000, v98
	v_mul_f32_e32 v99, 0x39800000, v99
	v_mul_f32_e32 v100, 0x39800000, v100
	v_mul_f32_e32 v101, 0x39800000, v101
	v_mul_f32_e32 v102, 0x39800000, v102
	v_mul_f32_e32 v103, 0x39800000, v103
	v_mul_f32_e32 v104, 0x39800000, v104
	v_mul_f32_e32 v105, 0x39800000, v105
	v_mul_f32_e32 v106, 0x39800000, v106
	v_mul_f32_e32 v107, 0x39800000, v107
	v_mul_f32_e32 v108, 0x39800000, v108
	v_mul_f32_e32 v109, 0x39800000, v109
	v_mul_f32_e32 v110, 0x39800000, v110
	v_mul_f32_e32 v111, 0x39800000, v111
	v_cvt_pk_f16_f32 v192, v96, v97
	v_cvt_pk_f16_f32 v193, v98, v99
	v_cvt_pk_f16_f32 v194, v100, v101
	v_cvt_pk_f16_f32 v195, v102, v103
	global_store_dwordx4 v219, v[192:195], s[12:13] offset:0 sc1
	v_cvt_pk_f16_f32 v196, v104, v105
	v_cvt_pk_f16_f32 v197, v106, v107
	v_cvt_pk_f16_f32 v198, v108, v109
	v_cvt_pk_f16_f32 v199, v110, v111
	global_store_dwordx4 v219, v[196:199], s[12:13] offset:1024 sc1
	v_mul_f32_e32 v112, 0x39800000, v112
	v_mul_f32_e32 v113, 0x39800000, v113
	v_mul_f32_e32 v114, 0x39800000, v114
	v_mul_f32_e32 v115, 0x39800000, v115
	v_mul_f32_e32 v116, 0x39800000, v116
	v_mul_f32_e32 v117, 0x39800000, v117
	v_mul_f32_e32 v118, 0x39800000, v118
	v_mul_f32_e32 v119, 0x39800000, v119
	v_mul_f32_e32 v120, 0x39800000, v120
	v_mul_f32_e32 v121, 0x39800000, v121
	v_mul_f32_e32 v122, 0x39800000, v122
	v_mul_f32_e32 v123, 0x39800000, v123
	v_mul_f32_e32 v124, 0x39800000, v124
	v_mul_f32_e32 v125, 0x39800000, v125
	v_mul_f32_e32 v126, 0x39800000, v126
	v_mul_f32_e32 v127, 0x39800000, v127
	v_cvt_pk_f16_f32 v200, v112, v113
	v_cvt_pk_f16_f32 v201, v114, v115
	v_cvt_pk_f16_f32 v202, v116, v117
	v_cvt_pk_f16_f32 v203, v118, v119
	global_store_dwordx4 v219, v[200:203], s[12:13] offset:2048 sc1
	v_cvt_pk_f16_f32 v204, v120, v121
	v_cvt_pk_f16_f32 v205, v122, v123
	v_cvt_pk_f16_f32 v206, v124, v125
	v_cvt_pk_f16_f32 v207, v126, v127
	global_store_dwordx4 v219, v[204:207], s[12:13] offset:3072 sc1
	s_endpgm
